# HGRN2 H1 state-update block: all 16 LDS operand reads prefetched into idle registers, decay multiplies under the reads, MFMAs back to back with counted lgkmcnt (on top of the scalar-split multiplies)
# baseline (speedup 1.0000x reference)
.LBB0_577:
	v_add_u32_e32 v46, s49, v72
	ds_read_b128 v[46:49], v46
	ds_read_b128 v[50:53], v99
	ds_read_b128 v[140:143], v99 offset:64
	ds_read_b128 v[172:175], v100
	ds_read_b128 v[176:179], v100 offset:64
	ds_read_b128 v[180:183], v100 offset:2304
	ds_read_b128 v[184:187], v100 offset:2368
	ds_read_b128 v[188:191], v100 offset:4608
	ds_read_b128 v[192:195], v100 offset:4672
	ds_read_b128 v[196:199], v100 offset:6912
	ds_read_b128 v[214:217], v100 offset:6976
	ds_read_b128 v[218:221], v100 offset:9216
	ds_read_b128 v[222:225], v100 offset:9280
	ds_read_b128 v[226:229], v100 offset:11520
	ds_read_b128 v[230:233], v100 offset:11584
	v_add_f32_e32 v105, v105, v138
	s_nop 2
	v_cvt_pk_bf16_f32 v138, v42, v43
	v_cvt_pk_bf16_f32 v139, v44, v45
	s_waitcnt lgkmcnt(14)
	v_mul_f32_e32 v46, 0x3fb8aa3b, v46
	v_mul_f32_e32 v47, 0x3fb8aa3b, v47
	v_mul_f32_e32 v48, 0x3fb8aa3b, v48
	v_mul_f32_e32 v49, 0x3fb8aa3b, v49
	v_exp_f32_e32 v148, v46
	v_exp_f32_e32 v149, v47
	v_exp_f32_e32 v150, v48
	v_exp_f32_e32 v151, v49
	s_nop 0
	v_mul_f32_e32 v14, v14, v148
	v_mul_f32_e32 v15, v15, v149
	v_mul_f32_e32 v10, v10, v148
	v_mul_f32_e32 v11, v11, v149
	v_mul_f32_e32 v16, v16, v150
	v_mul_f32_e32 v17, v17, v151
	v_mul_f32_e32 v12, v12, v150
	v_mul_f32_e32 v13, v13, v151
	v_mul_f32_e32 v8, v8, v150
	v_mul_f32_e32 v9, v9, v151
	v_mul_f32_e32 v6, v6, v148
	v_mul_f32_e32 v7, v7, v149
	v_mul_f32_e32 v32, v32, v150
	v_mul_f32_e32 v33, v33, v151
	v_mul_f32_e64 v30, v30, v148
	v_mul_f32_e64 v31, v31, v149
	v_mul_f32_e32 v28, v28, v150
	v_mul_f32_e32 v29, v29, v151
	v_mul_f32_e32 v26, v26, v148
	v_mul_f32_e32 v27, v27, v149
	v_mul_f32_e32 v24, v24, v150
	v_mul_f32_e32 v25, v25, v151
	v_mul_f32_e32 v22, v22, v148
	v_mul_f32_e32 v23, v23, v149
	v_mul_f32_e64 v4, v4, v150
	v_mul_f32_e64 v5, v5, v151
	v_mul_f32_e32 v2, v2, v148
	v_mul_f32_e32 v3, v3, v149
	v_mul_f32_e32 v20, v20, v150
	v_mul_f32_e32 v21, v21, v151
	v_mul_f32_e32 v18, v18, v148
	v_mul_f32_e32 v19, v19, v149
	s_nop 1
	s_waitcnt lgkmcnt(11)
	v_mfma_f32_16x16x32_bf16 v[14:17], v[50:53], v[172:175], v[14:17]
	s_waitcnt lgkmcnt(10)
	v_mfma_f32_16x16x32_bf16 v[14:17], v[140:143], v[176:179], v[14:17]
	ds_read_b128 v[234:237], v100 offset:13824
	ds_read_b128 v[238:241], v100 offset:13888
	s_waitcnt lgkmcnt(11)
	v_mfma_f32_16x16x32_bf16 v[10:13], v[50:53], v[180:183], v[10:13]
	s_waitcnt lgkmcnt(10)
	v_mfma_f32_16x16x32_bf16 v[10:13], v[140:143], v[184:187], v[10:13]
	ds_read_b128 v[202:205], v100 offset:16128
	ds_read_b128 v[206:209], v100 offset:16192
	s_waitcnt lgkmcnt(11)
	v_mfma_f32_16x16x32_bf16 v[6:9], v[50:53], v[188:191], v[6:9]
	s_waitcnt lgkmcnt(10)
	v_mfma_f32_16x16x32_bf16 v[6:9], v[140:143], v[192:195], v[6:9]
	s_add_u32 s0, s0, 0x10000
	s_waitcnt lgkmcnt(9)
	v_mfma_f32_16x16x32_bf16 v[30:33], v[50:53], v[196:199], v[30:33]
	s_addc_u32 s1, s1, 0
	s_cmp_eq_u32 s0, 0x100000
	s_waitcnt lgkmcnt(8)
	v_mfma_f32_16x16x32_bf16 v[30:33], v[140:143], v[214:217], v[30:33]
	s_waitcnt lgkmcnt(7)
	v_mfma_f32_16x16x32_bf16 v[26:29], v[50:53], v[218:221], v[26:29]
	s_waitcnt lgkmcnt(6)
	v_mfma_f32_16x16x32_bf16 v[26:29], v[140:143], v[222:225], v[26:29]
	s_waitcnt lgkmcnt(5)
	v_mfma_f32_16x16x32_bf16 v[22:25], v[50:53], v[226:229], v[22:25]
	s_waitcnt lgkmcnt(4)
	v_mfma_f32_16x16x32_bf16 v[22:25], v[140:143], v[230:233], v[22:25]
	s_waitcnt lgkmcnt(3)
	v_mfma_f32_16x16x32_bf16 v[18:21], v[50:53], v[234:237], v[18:21]
	s_waitcnt lgkmcnt(2)
	v_mfma_f32_16x16x32_bf16 v[18:21], v[140:143], v[238:241], v[18:21]
	s_waitcnt lgkmcnt(1)
	v_mfma_f32_16x16x32_bf16 v[2:5], v[50:53], v[202:205], v[2:5]
	s_waitcnt lgkmcnt(0)
	v_mfma_f32_16x16x32_bf16 v[2:5], v[140:143], v[206:209], v[2:5]
	v_add_co_u32_e32 v46, vcc, 0x3100c000, v68
	s_nop 1
	v_addc_co_u32_e32 v47, vcc, 0, v69, vcc
	global_store_dwordx2 v[46:47], v[138:139], off
	s_barrier
	s_cbranch_scc1 .LBB0_692
